# memKV V^T epilogue de-serialised: the 16 column rstd values are loaded and rsq'd once per tile instead of reloaded with a vmcnt(0) before each of the 16 stores
# speedup vs baseline: 1.0064x; 1.0040x over previous
; __device__ __forceinline__ u32x4 pack8(const f32x4 a, const f32x4 b) { u32x4 w; w.x = cvt_pk_bf16(a[0], a[1]); w.y = cvt_pk_bf16(a[2], a[3]); w.z = cvt_pk_bf16(b[0], b[1]); w.w = cvt_pk_bf16(b[2], b[3]); return w; }
; __device__ __forceinline__ float rstd_of1(const float* ss, int row) { return __builtin_amdgcn_rsqf(ss[row] * (1.f / 1024.f) + 1e-6f); }
;     __device__ __forceinline__ void operator()(const f32x4 (&acc)[2][2][4][2], const Unit& u, int wr, int wc, int fr, int fq) const {
;         asm volatile("" : "+v"(fr), "+v"(fq));
;         const bool isv = u.pm >= 4; const int l = isv ? ((u.pm - 8) >> 3) : ((u.pn - 4) >> 3);
;         const int pr = isv ? ((u.pm - 8) & 7) : u.pm, pc = isv ? u.pn : ((u.pn - 4) & 7);
;         bf16_t* O = (isv ? MEMVT : MEMK) + (size_t)l * 1024 * 1024;
;         const int row0 = pr * BM + wr * 64 + fr, col0 = pc * BM + wc * 32 + fq * 8;
; #pragma unroll
;         for (int ai = 0; ai < 2; ++ai)
; #pragma unroll
;             for (int m = 0; m < 4; ++m) { const int row = row0 + ai * HALF + m * 16; const float rsr = isv ? 1.f : rstd_of1(mss, row);
; #pragma unroll
;                 for (int bj = 0; bj < 2; ++bj) { f32x4 a = acc[ai][bj][m][0] * rsr, b = acc[ai][bj][m][1] * rsr;
;                     if (isv) {
; #pragma unroll
;                         for (int j = 0; j < 4; ++j) { a[j] *= rstd_of1(mss, col0 + bj * HALF + j); b[j] *= rstd_of1(mss, col0 + bj * HALF + 4 + j); } }
;                     *(u32x4*)(O + (size_t)row * 1024 + col0 + bj * HALF) = pack8(a, b); } asm volatile("" ::: "memory"); }
.LBB0_607:
	s_and_b32 s4, s72, 7
	s_sub_i32 s42, s72, 24
	s_xor_b32 s43, s4, 4
	s_and_b64 s[4:5], s[44:45], exec
	s_cselect_b32 s4, s42, s43
	s_lshl_b32 s4, s4, 8
	s_or_b32 s4, s4, s59
	v_lshl_add_u32 v132, v132, 3, s4
	v_cndmask_b32_e64 v136, 0, 1, s[44:45]
	v_ashrrev_i32_e32 v133, 31, v132
	v_pk_mul_f32 v[142:143], v[130:131], v[138:139] op_sel_hi:[1,0]
	v_pk_mul_f32 v[146:147], v[128:129], v[138:139] op_sel_hi:[1,0]
	v_pk_mul_f32 v[144:145], v[126:127], v[138:139] op_sel_hi:[1,0]
	v_cmp_ne_u32_e64 s[42:43], 1, v136
	s_andn2_b64 vcc, exec, s[44:45]
	v_pk_mul_f32 v[148:149], v[124:125], v[138:139] op_sel_hi:[1,0]
	s_cbranch_vccnz .LBB0_609
	v_lshl_add_u64 v[136:137], v[132:133], 2, s[52:53]
	global_load_dwordx4 v[228:231], v[136:137], off
	global_load_dwordx4 v[232:235], v[136:137], off offset:16
	global_load_dwordx4 v[236:239], v[136:137], off offset:512
	global_load_dwordx4 v[240:243], v[136:137], off offset:528
	s_waitcnt vmcnt(0)
	v_fmamk_f32 v228, v228, 0x3a800000, v227
	v_fmamk_f32 v229, v229, 0x3a800000, v227
	v_fmamk_f32 v230, v230, 0x3a800000, v227
	v_fmamk_f32 v231, v231, 0x3a800000, v227
	v_fmamk_f32 v232, v232, 0x3a800000, v227
	v_fmamk_f32 v233, v233, 0x3a800000, v227
	v_fmamk_f32 v234, v234, 0x3a800000, v227
	v_fmamk_f32 v235, v235, 0x3a800000, v227
	v_fmamk_f32 v236, v236, 0x3a800000, v227
	v_fmamk_f32 v237, v237, 0x3a800000, v227
	v_fmamk_f32 v238, v238, 0x3a800000, v227
	v_fmamk_f32 v239, v239, 0x3a800000, v227
	v_fmamk_f32 v240, v240, 0x3a800000, v227
	v_fmamk_f32 v241, v241, 0x3a800000, v227
	v_fmamk_f32 v242, v242, 0x3a800000, v227
	v_fmamk_f32 v243, v243, 0x3a800000, v227
	v_rsq_f32_e32 v228, v228
	v_rsq_f32_e32 v229, v229
	v_rsq_f32_e32 v230, v230
	v_rsq_f32_e32 v231, v231
	v_rsq_f32_e32 v232, v232
	v_rsq_f32_e32 v233, v233
	v_rsq_f32_e32 v234, v234
	v_rsq_f32_e32 v235, v235
	v_rsq_f32_e32 v236, v236
	v_rsq_f32_e32 v237, v237
	v_rsq_f32_e32 v238, v238
	v_rsq_f32_e32 v239, v239
	v_rsq_f32_e32 v240, v240
	v_rsq_f32_e32 v241, v241
	v_rsq_f32_e32 v242, v242
	v_rsq_f32_e32 v243, v243
	s_nop 0
	v_pk_mul_f32 v[142:143], v[142:143], v[230:231]
	v_pk_mul_f32 v[146:147], v[146:147], v[228:229]
	v_pk_mul_f32 v[144:145], v[144:145], v[234:235]
	v_pk_mul_f32 v[148:149], v[148:149], v[232:233]
.LBB0_609:
	s_sub_i32 s75, s73, 32
	s_sub_i32 s77, s72, 28
	s_and_b64 s[4:5], s[44:45], exec
	s_cselect_b32 s4, s75, s77
	s_ashr_i32 s4, s4, 3
	s_and_b64 s[44:45], s[44:45], exec
	s_mov_b32 s5, 0x1a00000
	s_cselect_b32 s5, s5, 0x1600000
	s_add_u32 s44, s38, s5
	s_addc_u32 s45, s39, 0
	s_ashr_i32 s5, s4, 31
	s_lshl_b64 s[4:5], s[4:5], 21
	s_add_u32 s4, s44, s4
	s_addc_u32 s5, s45, s5
	v_lshl_add_u64 v[136:137], v[132:133], 1, s[4:5]
	v_lshlrev_b64 v[140:141], 11, v[134:135]
	v_mov_b32_e32 v139, v138
	v_lshl_add_u64 v[140:141], v[136:137], 0, v[140:141]
	v_cvt_pk_bf16_f32 v146, v146, v147
	v_cvt_pk_bf16_f32 v147, v142, v143
	v_cvt_pk_bf16_f32 v148, v148, v149
	v_cvt_pk_bf16_f32 v149, v144, v145
	v_mov_b32_e32 v144, v138
	v_mov_b32_e32 v145, v138
	global_store_dwordx4 v[140:141], v[146:149], off
	v_pk_mul_f32 v[142:143], v[122:123], v[144:145]
	v_pk_mul_f32 v[144:145], v[118:119], v[144:145]
	v_pk_mul_f32 v[146:147], v[120:121], v[138:139]
	s_and_b64 vcc, exec, s[42:43]
	v_pk_mul_f32 v[138:139], v[116:117], v[138:139]
	s_cbranch_vccnz .LBB0_611
	v_lshl_add_u64 v[152:153], v[132:133], 2, s[52:53]
	v_pk_mul_f32 v[142:143], v[142:143], v[238:239]
	v_pk_mul_f32 v[146:147], v[146:147], v[236:237]
	v_pk_mul_f32 v[144:145], v[144:145], v[242:243]
	v_pk_mul_f32 v[138:139], v[138:139], v[240:241]

; __device__ __forceinline__ u32x4 pack8(const f32x4 a, const f32x4 b) { u32x4 w; w.x = cvt_pk_bf16(a[0], a[1]); w.y = cvt_pk_bf16(a[2], a[3]); w.z = cvt_pk_bf16(b[0], b[1]); w.w = cvt_pk_bf16(b[2], b[3]); return w; }
; __device__ __forceinline__ float rstd_of1(const float* ss, int row) { return __builtin_amdgcn_rsqf(ss[row] * (1.f / 1024.f) + 1e-6f); }
;     __device__ __forceinline__ void operator()(const f32x4 (&acc)[2][2][4][2], const Unit& u, int wr, int wc, int fr, int fq) const {
;     ...
;             for (int m = 0; m < 4; ++m) { const int row = row0 + ai * HALF + m * 16; const float rsr = isv ? 1.f : rstd_of1(mss, row);
; #pragma unroll
;                 for (int bj = 0; bj < 2; ++bj) { f32x4 a = acc[ai][bj][m][0] * rsr, b = acc[ai][bj][m][1] * rsr;
;                     if (isv) {
; #pragma unroll
;                         for (int j = 0; j < 4; ++j) { a[j] *= rstd_of1(mss, col0 + bj * HALF + j); b[j] *= rstd_of1(mss, col0 + bj * HALF + 4 + j); } }
;                     *(u32x4*)(O + (size_t)row * 1024 + col0 + bj * HALF) = pack8(a, b); } asm volatile("" ::: "memory"); }
.LBB0_613:
	s_nop 0
	v_pk_mul_f32 v[142:143], v[114:115], v[138:139] op_sel_hi:[1,0]
	v_pk_mul_f32 v[146:147], v[112:113], v[138:139] op_sel_hi:[1,0]
	v_pk_mul_f32 v[144:145], v[110:111], v[138:139] op_sel_hi:[1,0]
	s_and_b64 vcc, exec, s[42:43]
	v_pk_mul_f32 v[148:149], v[108:109], v[138:139] op_sel_hi:[1,0]
	s_cbranch_vccnz .LBB0_615
	v_lshl_add_u64 v[154:155], v[132:133], 2, s[52:53]
	v_pk_mul_f32 v[142:143], v[142:143], v[230:231]
	v_pk_mul_f32 v[146:147], v[146:147], v[228:229]
	v_pk_mul_f32 v[144:145], v[144:145], v[234:235]
	v_pk_mul_f32 v[148:149], v[148:149], v[232:233]
.LBB0_615:
	v_lshlrev_b64 v[140:141], 11, v[140:141]
	v_mov_b32_e32 v139, v138
	v_lshl_add_u64 v[140:141], v[136:137], 0, v[140:141]
	v_cvt_pk_bf16_f32 v146, v146, v147
	v_cvt_pk_bf16_f32 v147, v142, v143
	v_cvt_pk_bf16_f32 v148, v148, v149
	v_cvt_pk_bf16_f32 v149, v144, v145
	v_mov_b32_e32 v144, v138
	v_mov_b32_e32 v145, v138
	global_store_dwordx4 v[140:141], v[146:149], off
	v_pk_mul_f32 v[142:143], v[106:107], v[144:145]
	v_pk_mul_f32 v[144:145], v[102:103], v[144:145]
	v_pk_mul_f32 v[146:147], v[104:105], v[138:139]
	s_and_b64 vcc, exec, s[42:43]
	v_pk_mul_f32 v[138:139], v[100:101], v[138:139]
	s_cbranch_vccnz .LBB0_617
	v_lshl_add_u64 v[152:153], v[132:133], 2, s[52:53]
	v_pk_mul_f32 v[142:143], v[142:143], v[238:239]
	v_pk_mul_f32 v[146:147], v[146:147], v[236:237]
	v_pk_mul_f32 v[144:145], v[144:145], v[242:243]
	v_pk_mul_f32 v[138:139], v[138:139], v[240:241]

; __device__ __forceinline__ u32x4 pack8(const f32x4 a, const f32x4 b) { u32x4 w; w.x = cvt_pk_bf16(a[0], a[1]); w.y = cvt_pk_bf16(a[2], a[3]); w.z = cvt_pk_bf16(b[0], b[1]); w.w = cvt_pk_bf16(b[2], b[3]); return w; }
; __device__ __forceinline__ float rstd_of1(const float* ss, int row) { return __builtin_amdgcn_rsqf(ss[row] * (1.f / 1024.f) + 1e-6f); }
;     __device__ __forceinline__ void operator()(const f32x4 (&acc)[2][2][4][2], const Unit& u, int wr, int wc, int fr, int fq) const {
;     ...
;             for (int m = 0; m < 4; ++m) { const int row = row0 + ai * HALF + m * 16; const float rsr = isv ? 1.f : rstd_of1(mss, row);
; #pragma unroll
;                 for (int bj = 0; bj < 2; ++bj) { f32x4 a = acc[ai][bj][m][0] * rsr, b = acc[ai][bj][m][1] * rsr;
;                     if (isv) {
; #pragma unroll
;                         for (int j = 0; j < 4; ++j) { a[j] *= rstd_of1(mss, col0 + bj * HALF + j); b[j] *= rstd_of1(mss, col0 + bj * HALF + 4 + j); } }
;                     *(u32x4*)(O + (size_t)row * 1024 + col0 + bj * HALF) = pack8(a, b); } asm volatile("" ::: "memory"); }
.LBB0_619:
	s_nop 0
	v_pk_mul_f32 v[142:143], v[98:99], v[138:139] op_sel_hi:[1,0]
	v_pk_mul_f32 v[146:147], v[96:97], v[138:139] op_sel_hi:[1,0]
	v_pk_mul_f32 v[144:145], v[94:95], v[138:139] op_sel_hi:[1,0]
	s_and_b64 vcc, exec, s[42:43]
	v_pk_mul_f32 v[148:149], v[92:93], v[138:139] op_sel_hi:[1,0]
	s_cbranch_vccnz .LBB0_621
	v_lshl_add_u64 v[154:155], v[132:133], 2, s[52:53]
	v_pk_mul_f32 v[142:143], v[142:143], v[230:231]
	v_pk_mul_f32 v[146:147], v[146:147], v[228:229]
	v_pk_mul_f32 v[144:145], v[144:145], v[234:235]
	v_pk_mul_f32 v[148:149], v[148:149], v[232:233]
.LBB0_621:
	v_lshlrev_b64 v[140:141], 11, v[140:141]
	v_mov_b32_e32 v139, v138
	v_lshl_add_u64 v[140:141], v[136:137], 0, v[140:141]
	v_cvt_pk_bf16_f32 v146, v146, v147
	v_cvt_pk_bf16_f32 v147, v142, v143
	v_cvt_pk_bf16_f32 v148, v148, v149
	v_cvt_pk_bf16_f32 v149, v144, v145
	v_mov_b32_e32 v144, v138
	v_mov_b32_e32 v145, v138
	global_store_dwordx4 v[140:141], v[146:149], off
	v_pk_mul_f32 v[142:143], v[90:91], v[144:145]
	v_pk_mul_f32 v[144:145], v[86:87], v[144:145]
	v_pk_mul_f32 v[146:147], v[88:89], v[138:139]
	s_and_b64 vcc, exec, s[42:43]
	v_pk_mul_f32 v[138:139], v[84:85], v[138:139]
	s_cbranch_vccnz .LBB0_623
	v_lshl_add_u64 v[152:153], v[132:133], 2, s[52:53]
	v_pk_mul_f32 v[142:143], v[142:143], v[238:239]
	v_pk_mul_f32 v[146:147], v[146:147], v[236:237]
	v_pk_mul_f32 v[144:145], v[144:145], v[242:243]
	v_pk_mul_f32 v[138:139], v[138:139], v[240:241]

; __device__ __forceinline__ u32x4 pack8(const f32x4 a, const f32x4 b) { u32x4 w; w.x = cvt_pk_bf16(a[0], a[1]); w.y = cvt_pk_bf16(a[2], a[3]); w.z = cvt_pk_bf16(b[0], b[1]); w.w = cvt_pk_bf16(b[2], b[3]); return w; }
; __device__ __forceinline__ float rstd_of1(const float* ss, int row) { return __builtin_amdgcn_rsqf(ss[row] * (1.f / 1024.f) + 1e-6f); }
;     __device__ __forceinline__ void operator()(const f32x4 (&acc)[2][2][4][2], const Unit& u, int wr, int wc, int fr, int fq) const {
;     ...
;             for (int m = 0; m < 4; ++m) { const int row = row0 + ai * HALF + m * 16; const float rsr = isv ? 1.f : rstd_of1(mss, row);
; #pragma unroll
;                 for (int bj = 0; bj < 2; ++bj) { f32x4 a = acc[ai][bj][m][0] * rsr, b = acc[ai][bj][m][1] * rsr;
;                     if (isv) {
; #pragma unroll
;                         for (int j = 0; j < 4; ++j) { a[j] *= rstd_of1(mss, col0 + bj * HALF + j); b[j] *= rstd_of1(mss, col0 + bj * HALF + 4 + j); } }
;                     *(u32x4*)(O + (size_t)row * 1024 + col0 + bj * HALF) = pack8(a, b); } asm volatile("" ::: "memory"); }
.LBB0_625:
	s_nop 0
	v_pk_mul_f32 v[142:143], v[82:83], v[138:139] op_sel_hi:[1,0]
	v_pk_mul_f32 v[146:147], v[80:81], v[138:139] op_sel_hi:[1,0]
	v_pk_mul_f32 v[144:145], v[78:79], v[138:139] op_sel_hi:[1,0]
	s_and_b64 vcc, exec, s[42:43]
	v_pk_mul_f32 v[148:149], v[76:77], v[138:139] op_sel_hi:[1,0]
	s_cbranch_vccnz .LBB0_627
	v_lshl_add_u64 v[154:155], v[132:133], 2, s[52:53]
	v_pk_mul_f32 v[142:143], v[142:143], v[230:231]
	v_pk_mul_f32 v[146:147], v[146:147], v[228:229]
	v_pk_mul_f32 v[144:145], v[144:145], v[234:235]
	v_pk_mul_f32 v[148:149], v[148:149], v[232:233]
.LBB0_627:
	v_lshlrev_b64 v[140:141], 11, v[140:141]
	v_mov_b32_e32 v139, v138
	v_lshl_add_u64 v[140:141], v[136:137], 0, v[140:141]
	v_cvt_pk_bf16_f32 v146, v146, v147
	v_cvt_pk_bf16_f32 v147, v142, v143
	v_cvt_pk_bf16_f32 v148, v148, v149
	v_cvt_pk_bf16_f32 v149, v144, v145
	v_mov_b32_e32 v144, v138
	v_mov_b32_e32 v145, v138
	global_store_dwordx4 v[140:141], v[146:149], off
	v_pk_mul_f32 v[142:143], v[74:75], v[144:145]
	v_pk_mul_f32 v[144:145], v[70:71], v[144:145]
	v_pk_mul_f32 v[146:147], v[72:73], v[138:139]
	s_and_b64 vcc, exec, s[42:43]
	v_pk_mul_f32 v[138:139], v[68:69], v[138:139]
	s_cbranch_vccnz .LBB0_629
	v_lshl_add_u64 v[152:153], v[132:133], 2, s[52:53]
	v_pk_mul_f32 v[142:143], v[142:143], v[238:239]
	v_pk_mul_f32 v[146:147], v[146:147], v[236:237]
	v_pk_mul_f32 v[144:145], v[144:145], v[242:243]
	v_pk_mul_f32 v[138:139], v[138:139], v[240:241]

; __device__ __forceinline__ u32x4 pack8(const f32x4 a, const f32x4 b) { u32x4 w; w.x = cvt_pk_bf16(a[0], a[1]); w.y = cvt_pk_bf16(a[2], a[3]); w.z = cvt_pk_bf16(b[0], b[1]); w.w = cvt_pk_bf16(b[2], b[3]); return w; }
; __device__ __forceinline__ float rstd_of1(const float* ss, int row) { return __builtin_amdgcn_rsqf(ss[row] * (1.f / 1024.f) + 1e-6f); }
;     __device__ __forceinline__ void operator()(const f32x4 (&acc)[2][2][4][2], const Unit& u, int wr, int wc, int fr, int fq) const {
;     ...
;             for (int m = 0; m < 4; ++m) { const int row = row0 + ai * HALF + m * 16; const float rsr = isv ? 1.f : rstd_of1(mss, row);
; #pragma unroll
;                 for (int bj = 0; bj < 2; ++bj) { f32x4 a = acc[ai][bj][m][0] * rsr, b = acc[ai][bj][m][1] * rsr;
;                     if (isv) {
; #pragma unroll
;                         for (int j = 0; j < 4; ++j) { a[j] *= rstd_of1(mss, col0 + bj * HALF + j); b[j] *= rstd_of1(mss, col0 + bj * HALF + 4 + j); } }
;                     *(u32x4*)(O + (size_t)row * 1024 + col0 + bj * HALF) = pack8(a, b); } asm volatile("" ::: "memory"); }
.LBB0_631:
	s_nop 0
	v_pk_mul_f32 v[142:143], v[66:67], v[138:139] op_sel_hi:[1,0]
	v_pk_mul_f32 v[146:147], v[64:65], v[138:139] op_sel_hi:[1,0]
	v_pk_mul_f32 v[144:145], v[62:63], v[138:139] op_sel_hi:[1,0]
	s_and_b64 vcc, exec, s[42:43]
	v_pk_mul_f32 v[148:149], v[60:61], v[138:139] op_sel_hi:[1,0]
	s_cbranch_vccnz .LBB0_633
	v_lshl_add_u64 v[154:155], v[132:133], 2, s[52:53]
	v_pk_mul_f32 v[142:143], v[142:143], v[230:231]
	v_pk_mul_f32 v[146:147], v[146:147], v[228:229]
	v_pk_mul_f32 v[144:145], v[144:145], v[234:235]
	v_pk_mul_f32 v[148:149], v[148:149], v[232:233]
.LBB0_633:
	v_lshlrev_b64 v[140:141], 11, v[140:141]
	v_mov_b32_e32 v139, v138
	v_lshl_add_u64 v[140:141], v[136:137], 0, v[140:141]
	v_cvt_pk_bf16_f32 v146, v146, v147
	v_cvt_pk_bf16_f32 v147, v142, v143
	v_cvt_pk_bf16_f32 v148, v148, v149
	v_cvt_pk_bf16_f32 v149, v144, v145
	v_mov_b32_e32 v144, v138
	v_mov_b32_e32 v145, v138
	global_store_dwordx4 v[140:141], v[146:149], off
	v_pk_mul_f32 v[142:143], v[58:59], v[144:145]
	v_pk_mul_f32 v[144:145], v[54:55], v[144:145]
	v_pk_mul_f32 v[146:147], v[56:57], v[138:139]
	s_and_b64 vcc, exec, s[42:43]
	v_pk_mul_f32 v[138:139], v[52:53], v[138:139]
	s_cbranch_vccnz .LBB0_635
	v_lshl_add_u64 v[152:153], v[132:133], 2, s[52:53]
	v_pk_mul_f32 v[142:143], v[142:143], v[238:239]
	v_pk_mul_f32 v[146:147], v[146:147], v[236:237]
	v_pk_mul_f32 v[144:145], v[144:145], v[242:243]
	v_pk_mul_f32 v[138:139], v[138:139], v[240:241]

; __device__ __forceinline__ u32x4 pack8(const f32x4 a, const f32x4 b) { u32x4 w; w.x = cvt_pk_bf16(a[0], a[1]); w.y = cvt_pk_bf16(a[2], a[3]); w.z = cvt_pk_bf16(b[0], b[1]); w.w = cvt_pk_bf16(b[2], b[3]); return w; }
; __device__ __forceinline__ float rstd_of1(const float* ss, int row) { return __builtin_amdgcn_rsqf(ss[row] * (1.f / 1024.f) + 1e-6f); }
;     __device__ __forceinline__ void operator()(const f32x4 (&acc)[2][2][4][2], const Unit& u, int wr, int wc, int fr, int fq) const {
;     ...
;             for (int m = 0; m < 4; ++m) { const int row = row0 + ai * HALF + m * 16; const float rsr = isv ? 1.f : rstd_of1(mss, row);
; #pragma unroll
;                 for (int bj = 0; bj < 2; ++bj) { f32x4 a = acc[ai][bj][m][0] * rsr, b = acc[ai][bj][m][1] * rsr;
;                     if (isv) {
; #pragma unroll
;                         for (int j = 0; j < 4; ++j) { a[j] *= rstd_of1(mss, col0 + bj * HALF + j); b[j] *= rstd_of1(mss, col0 + bj * HALF + 4 + j); } }
;                     *(u32x4*)(O + (size_t)row * 1024 + col0 + bj * HALF) = pack8(a, b); } asm volatile("" ::: "memory"); }
.LBB0_637:
	s_nop 0
	v_pk_mul_f32 v[142:143], v[50:51], v[138:139] op_sel_hi:[1,0]
	v_pk_mul_f32 v[146:147], v[48:49], v[138:139] op_sel_hi:[1,0]
	v_pk_mul_f32 v[144:145], v[46:47], v[138:139] op_sel_hi:[1,0]
	s_and_b64 vcc, exec, s[42:43]
	v_pk_mul_f32 v[148:149], v[44:45], v[138:139] op_sel_hi:[1,0]
	s_cbranch_vccnz .LBB0_639
	v_lshl_add_u64 v[154:155], v[132:133], 2, s[52:53]
	v_pk_mul_f32 v[142:143], v[142:143], v[230:231]
	v_pk_mul_f32 v[146:147], v[146:147], v[228:229]
	v_pk_mul_f32 v[144:145], v[144:145], v[234:235]
	v_pk_mul_f32 v[148:149], v[148:149], v[232:233]
.LBB0_639:
	v_lshlrev_b64 v[140:141], 11, v[140:141]
	v_mov_b32_e32 v139, v138
	v_lshl_add_u64 v[140:141], v[136:137], 0, v[140:141]
	v_cvt_pk_bf16_f32 v146, v146, v147
	v_cvt_pk_bf16_f32 v147, v142, v143
	v_cvt_pk_bf16_f32 v148, v148, v149
	v_cvt_pk_bf16_f32 v149, v144, v145
	v_mov_b32_e32 v144, v138
	v_mov_b32_e32 v145, v138
	global_store_dwordx4 v[140:141], v[146:149], off
	v_pk_mul_f32 v[142:143], v[42:43], v[144:145]
	v_pk_mul_f32 v[144:145], v[38:39], v[144:145]
	v_pk_mul_f32 v[146:147], v[40:41], v[138:139]
	s_and_b64 vcc, exec, s[42:43]
	v_pk_mul_f32 v[138:139], v[36:37], v[138:139]
	s_cbranch_vccnz .LBB0_641
	v_lshl_add_u64 v[152:153], v[132:133], 2, s[52:53]
	v_pk_mul_f32 v[142:143], v[142:143], v[238:239]
	v_pk_mul_f32 v[146:147], v[146:147], v[236:237]
	v_pk_mul_f32 v[144:145], v[144:145], v[242:243]
	v_pk_mul_f32 v[138:139], v[138:139], v[240:241]

; __device__ __forceinline__ u32x4 pack8(const f32x4 a, const f32x4 b) { u32x4 w; w.x = cvt_pk_bf16(a[0], a[1]); w.y = cvt_pk_bf16(a[2], a[3]); w.z = cvt_pk_bf16(b[0], b[1]); w.w = cvt_pk_bf16(b[2], b[3]); return w; }
; __device__ __forceinline__ float rstd_of1(const float* ss, int row) { return __builtin_amdgcn_rsqf(ss[row] * (1.f / 1024.f) + 1e-6f); }
;     __device__ __forceinline__ void operator()(const f32x4 (&acc)[2][2][4][2], const Unit& u, int wr, int wc, int fr, int fq) const {
;     ...
;             for (int m = 0; m < 4; ++m) { const int row = row0 + ai * HALF + m * 16; const float rsr = isv ? 1.f : rstd_of1(mss, row);
; #pragma unroll
;                 for (int bj = 0; bj < 2; ++bj) { f32x4 a = acc[ai][bj][m][0] * rsr, b = acc[ai][bj][m][1] * rsr;
;                     if (isv) {
; #pragma unroll
;                         for (int j = 0; j < 4; ++j) { a[j] *= rstd_of1(mss, col0 + bj * HALF + j); b[j] *= rstd_of1(mss, col0 + bj * HALF + 4 + j); } }
;                     *(u32x4*)(O + (size_t)row * 1024 + col0 + bj * HALF) = pack8(a, b); } asm volatile("" ::: "memory"); }
.LBB0_643:
	s_nop 0
	v_pk_mul_f32 v[142:143], v[34:35], v[138:139] op_sel_hi:[1,0]
	v_pk_mul_f32 v[146:147], v[32:33], v[138:139] op_sel_hi:[1,0]
	v_pk_mul_f32 v[144:145], v[30:31], v[138:139] op_sel_hi:[1,0]
	s_and_b64 vcc, exec, s[42:43]
	v_pk_mul_f32 v[148:149], v[28:29], v[138:139] op_sel_hi:[1,0]
	s_cbranch_vccnz .LBB0_645
	v_lshl_add_u64 v[154:155], v[132:133], 2, s[52:53]
	v_pk_mul_f32 v[142:143], v[142:143], v[230:231]
	v_pk_mul_f32 v[146:147], v[146:147], v[228:229]
	v_pk_mul_f32 v[144:145], v[144:145], v[234:235]
	v_pk_mul_f32 v[148:149], v[148:149], v[232:233]
.LBB0_645:
	v_lshlrev_b64 v[140:141], 11, v[140:141]
	v_mov_b32_e32 v139, v138
	v_lshl_add_u64 v[140:141], v[136:137], 0, v[140:141]
	v_cvt_pk_bf16_f32 v146, v146, v147
	v_cvt_pk_bf16_f32 v147, v142, v143
	v_cvt_pk_bf16_f32 v148, v148, v149
	v_cvt_pk_bf16_f32 v149, v144, v145
	v_mov_b32_e32 v144, v138
	v_mov_b32_e32 v145, v138
	global_store_dwordx4 v[140:141], v[146:149], off
	v_pk_mul_f32 v[142:143], v[26:27], v[144:145]
	v_pk_mul_f32 v[144:145], v[22:23], v[144:145]
	v_pk_mul_f32 v[146:147], v[24:25], v[138:139]
	s_and_b64 vcc, exec, s[42:43]
	v_pk_mul_f32 v[138:139], v[20:21], v[138:139]
	s_cbranch_vccnz .LBB0_647
	v_lshl_add_u64 v[152:153], v[132:133], 2, s[52:53]
	v_pk_mul_f32 v[142:143], v[142:143], v[238:239]
	v_pk_mul_f32 v[146:147], v[146:147], v[236:237]
	v_pk_mul_f32 v[144:145], v[144:145], v[242:243]
	v_pk_mul_f32 v[138:139], v[138:139], v[240:241]

; __device__ __forceinline__ u32x4 pack8(const f32x4 a, const f32x4 b) { u32x4 w; w.x = cvt_pk_bf16(a[0], a[1]); w.y = cvt_pk_bf16(a[2], a[3]); w.z = cvt_pk_bf16(b[0], b[1]); w.w = cvt_pk_bf16(b[2], b[3]); return w; }
; __device__ __forceinline__ float rstd_of1(const float* ss, int row) { return __builtin_amdgcn_rsqf(ss[row] * (1.f / 1024.f) + 1e-6f); }
;     __device__ __forceinline__ void operator()(const f32x4 (&acc)[2][2][4][2], const Unit& u, int wr, int wc, int fr, int fq) const {
;     ...
;             for (int m = 0; m < 4; ++m) { const int row = row0 + ai * HALF + m * 16; const float rsr = isv ? 1.f : rstd_of1(mss, row);
; #pragma unroll
;                 for (int bj = 0; bj < 2; ++bj) { f32x4 a = acc[ai][bj][m][0] * rsr, b = acc[ai][bj][m][1] * rsr;
;                     if (isv) {
; #pragma unroll
;                         for (int j = 0; j < 4; ++j) { a[j] *= rstd_of1(mss, col0 + bj * HALF + j); b[j] *= rstd_of1(mss, col0 + bj * HALF + 4 + j); } }
;                     *(u32x4*)(O + (size_t)row * 1024 + col0 + bj * HALF) = pack8(a, b); } asm volatile("" ::: "memory"); }
.LBB0_649:
	s_nop 0
	v_pk_mul_f32 v[140:141], v[18:19], v[134:135] op_sel_hi:[1,0]
	v_pk_mul_f32 v[144:145], v[16:17], v[134:135] op_sel_hi:[1,0]
	v_pk_mul_f32 v[142:143], v[14:15], v[134:135] op_sel_hi:[1,0]
	s_and_b64 vcc, exec, s[42:43]
	v_pk_mul_f32 v[146:147], v[12:13], v[134:135] op_sel_hi:[1,0]
	s_cbranch_vccnz .LBB0_651
	v_lshl_add_u64 v[152:153], v[132:133], 2, s[52:53]
	v_pk_mul_f32 v[140:141], v[140:141], v[230:231]
	v_pk_mul_f32 v[144:145], v[144:145], v[228:229]
	v_pk_mul_f32 v[142:143], v[142:143], v[234:235]
	v_pk_mul_f32 v[146:147], v[146:147], v[232:233]
.LBB0_651:
	v_lshlrev_b64 v[138:139], 11, v[138:139]
	v_lshl_add_u64 v[136:137], v[136:137], 0, v[138:139]
	v_cvt_pk_bf16_f32 v138, v144, v145
	v_cvt_pk_bf16_f32 v139, v140, v141
	v_cvt_pk_bf16_f32 v140, v146, v147
	v_cvt_pk_bf16_f32 v141, v142, v143
	v_mov_b32_e32 v135, v134
	global_store_dwordx4 v[136:137], v[138:141], off
	v_pk_mul_f32 v[142:143], v[8:9], v[134:135]
	s_and_b64 vcc, exec, s[42:43]
	v_mov_b32_e32 v140, v134
	v_mov_b32_e32 v141, v134
	v_pk_mul_f32 v[138:139], v[10:11], v[140:141]
	v_pk_mul_f32 v[140:141], v[6:7], v[140:141]
	v_pk_mul_f32 v[134:135], v[4:5], v[134:135]
	s_cbranch_vccnz .LBB0_653
	v_lshl_add_u64 v[132:133], v[132:133], 2, s[52:53]
	v_pk_mul_f32 v[138:139], v[138:139], v[238:239]
	v_pk_mul_f32 v[142:143], v[142:143], v[236:237]
	v_pk_mul_f32 v[140:141], v[140:141], v[242:243]
	v_pk_mul_f32 v[134:135], v[134:135], v[240:241]
